# speedup vs baseline: 1.0044x; 1.0035x over previous
_Z6mainK2PKDF16_S0_S0_PKfPKiS4_S2_PfS0_S4_S4_:
	s_mov_b32 s92, 0x80
	s_load_dwordx2 s[20:21], s[0:1], 0x50
	s_load_dwordx2 s[24:25], s[0:1], 0x40
	s_load_dwordx2 s[58:59], s[0:1], 0x8
	s_load_dwordx2 s[90:91], s[0:1], 0x28
	v_readfirstlane_b32 s3, v0
	s_lshr_b32 s38, s3, 6
	s_lshl_b32 s2, s2, 3
	s_add_i32 s6, s38, s2
	s_cmpk_lt_i32 s6, 0x753
	v_and_b32_e32 v115, 15, v0
	v_mov_b32_e32 v106, -1
	s_cselect_b64 s[2:3], -1, 0
	s_cmpk_gt_i32 s6, 0x752
	v_mov_b32_e32 v108, -1
	s_cbranch_scc1 .LBB2_2
	s_load_dwordx2 s[4:5], s[0:1], 0x48
	v_lshl_or_b32 v2, s6, 4, v115
	v_ashrrev_i32_e32 v3, 31, v2
	s_waitcnt lgkmcnt(0)
	v_lshl_add_u64 v[2:3], v[2:3], 2, s[4:5]
	global_load_dword v108, v[2:3], off

.LBB2_58:
	v_mov_b32_e32 v187, 0x4138aa3b
	v_lshrrev_b32_e32 v38, 3, v115
	v_lshlrev_b32_e32 v40, 5, v0
	v_lshrrev_b32_e32 v107, 4, v110
	s_lshl_b32 s6, s38, 13
	v_and_or_b32 v38, v175, 2, v38
	v_and_b32_e32 v40, 0x180, v40
	v_lshlrev_b32_e32 v41, 3, v0
	s_add_i32 s6, s6, 0x12000
	v_lshlrev_b32_e32 v39, 9, v107
	v_and_or_b32 v40, v41, 24, v40
	v_lshlrev_b32_e32 v38, 5, v38
	v_lshrrev_b32_e32 v37, 3, v0
	v_or3_b32 v39, v40, v39, s6
	v_xor_b32_e32 v40, 32, v38
	v_lshl_add_u32 v191, v110, 5, s39
	v_and_b32_e32 v0, 7, v0
	v_or_b32_e32 v186, v39, v38
	v_or_b32_e32 v188, v39, v40
	v_xor_b32_e32 v40, 64, v38
	v_xor_b32_e32 v38, 0x60, v38
	v_bitop3_b32 v0, v37, v0, 6 bitop3:0x6c
	v_or_b32_e32 v190, v39, v38
	v_and_b32_e32 v1, 0x380, v122
	v_lshlrev_b32_e32 v38, 4, v0
	v_add_u32_e32 v0, s33, v115
	v_or_b32_e32 v189, v39, v40
	v_lshlrev_b32_e32 v34, 2, v34
	v_mov_b32_e32 v35, 0
	v_and_b32_e32 v122, 6, v115
	v_xor_b32_e32 v122, v122, v107
	v_lshlrev_b32_e32 v122, 4, v122
	v_lshl_add_u32 v122, v115, 7, v122
	v_add_u32_e32 v122, s6, v122
	s_mov_b32 s60, 0xffff0000
	s_mov_b32 s61, 0
	s_mov_b32 s62, 0
	s_mov_b32 s63, 0xffff
	s_mov_b32 s64, 0
	s_mov_b32 s65, 0xffff0000
	v_or_b32_e32 v39, s6, v1
	v_add_u32_e32 v192, 0x15f90, v0
	v_lshlrev_b32_e32 v0, 7, v107
	v_and_b32_e32 v1, 0x78, v41
	v_lshl_add_u64 v[126:127], s[30:31], 0, v[34:35]
	v_and_b32_e32 v200, 1, v114
	v_mul_u32_u24_e32 v200, 0x980, v200
	v_add_co_u32_e32 v126, vcc, v126, v200
	s_nop 1
	v_addc_co_u32_e32 v127, vcc, 0, v127, vcc
	v_or3_b32 v193, v1, v0, s39
	v_add_u32_e32 v0, s33, v110
	v_mov_b32_e32 v34, v116
	v_mov_b32_e32 v37, v35
	v_lshl_or_b32 v194, v110, 16, v0
	v_lshl_add_u64 v[0:1], v[34:35], 0, v[36:37]
	v_mov_b32_e32 v36, v35
	v_mov_b32_e32 v76, v35
	v_mov_b32_e32 v77, v35
	v_lshl_add_u64 v[0:1], s[34:35], 0, v[0:1]
	v_mov_b32_e32 v34, v35
	v_mov_b32_e32 v74, v35
	v_mov_b32_e32 v75, v35
	s_mov_b32 s12, 0x3c003c00
	v_mov_b64_e32 v[80:81], v[76:77]
	v_mov_b64_e32 v[84:85], v[76:77]
	v_mov_b64_e32 v[88:89], v[76:77]
	v_mov_b64_e32 v[92:93], v[76:77]
	v_mov_b64_e32 v[96:97], v[76:77]
	v_mov_b64_e32 v[100:101], v[76:77]
	v_mov_b64_e32 v[104:105], v[76:77]
	v_mov_b64_e32 v[56:57], v[36:37]
	v_mov_b64_e32 v[60:61], v[36:37]
	v_mov_b64_e32 v[64:65], v[36:37]
	v_mov_b64_e32 v[68:69], v[36:37]
	v_mov_b64_e32 v[72:73], v[36:37]
	s_or_b32 s47, s40, 0x80
	v_lshl_add_u64 v[0:1], v[0:1], 0, 64
	s_mov_b32 s49, 0
	s_mov_b64 s[30:31], -1
	s_mov_b32 s13, s12
	s_movk_i32 s48, 0x300
	v_lshl_add_u32 v118, v114, 4, v116
	v_mov_b32_e32 v119, v165
	v_mov_b32_e32 v116, 0xc3500
	v_lshlrev_b32_e32 v128, 2, v114
	v_add_u32_e32 v196, v39, v38
	v_mov_b64_e32 v[78:79], v[74:75]
	v_mov_b64_e32 v[82:83], v[74:75]
	v_mov_b64_e32 v[86:87], v[74:75]
	v_mov_b64_e32 v[90:91], v[74:75]
	v_mov_b64_e32 v[94:95], v[74:75]
	v_mov_b64_e32 v[98:99], v[74:75]
	v_mov_b64_e32 v[102:103], v[74:75]
	v_mov_b64_e32 v[54:55], v[34:35]
	v_mov_b64_e32 v[58:59], v[34:35]
	v_mov_b64_e32 v[62:63], v[34:35]
	v_mov_b64_e32 v[66:67], v[34:35]
	s_mov_b32 s50, 0
	v_mov_b64_e32 v[70:71], v[34:35]
	v_mov_b32_e32 v50, v35
	v_mov_b32_e32 v51, v35
	v_mov_b32_e32 v52, v35
	v_mov_b32_e32 v53, v35
	v_mov_b32_e32 v46, v35
	v_mov_b32_e32 v47, v35
	v_mov_b32_e32 v48, v35
	v_mov_b32_e32 v49, v35
	v_mov_b32_e32 v42, v35
	v_mov_b32_e32 v43, v35
	v_mov_b32_e32 v44, v35
	v_mov_b32_e32 v45, v35
	v_mov_b32_e32 v38, v35
	v_mov_b32_e32 v39, v35
	v_mov_b32_e32 v40, v35
	v_mov_b32_e32 v41, v35
	s_waitcnt vmcnt(0)
	ds_write_b128 v196, v[10:13]
	ds_write_b128 v196, v[14:17] offset:1024
	ds_write_b128 v196, v[30:33] offset:2048
	ds_write_b128 v196, v[26:29] offset:3072
	ds_write_b128 v196, v[2:5] offset:4096
	ds_write_b128 v196, v[6:9] offset:5120
	ds_write_b128 v196, v[18:21] offset:6144
	ds_write_b128 v196, v[22:25] offset:7168
	s_mul_i32 s78, s42, 0xc00
	s_add_i32 s78, s78, s40
	v_mov_b32_e32 v183, v121
	s_lshl_b32 s6, s43, 6
	s_sub_i32 s83, s44, s6
	s_lshl_b32 s6, s43, 8
	s_add_i32 s82, s78, s6
	v_add_u32_e32 v229, s82, v172
	v_add_u32_e32 v230, s82, v173
	ds_read2_b32 v[224:225], v229 offset1:8
	ds_read2_b32 v[226:227], v229 offset0:16 offset1:24
	ds_read2_b32 v[232:233], v229 offset0:32 offset1:40
	ds_read2_b32 v[234:235], v229 offset0:48 offset1:56
	ds_read_b32 v183, v230
	s_waitcnt lgkmcnt(0)
	s_mov_b32 s85, s83
.Lmk_pg:
	s_cmp_gt_i32 s83, 32
	v_mad_u32_u16 v10, v224, s92, v176
	v_mad_u32_u16 v14, v225, s92, v176
	s_cselect_b64 s[30:31], -1, 0
	v_mad_u32_u16 v30, v226, s92, v176
	v_mad_u32_u16 v26, v227, s92, v176
	s_cmp_lt_i32 s83, 33
	global_load_dwordx4 v[10:13], v10, s[28:29]
	global_load_dwordx4 v[14:17], v14, s[28:29]
	global_load_dwordx4 v[30:33], v30, s[28:29]
	global_load_dwordx4 v[26:29], v26, s[28:29]
	s_cbranch_scc1 .Lmk_p68
	v_mad_u32_u16 v2, v232, s92, v176
	v_mad_u32_u16 v6, v233, s92, v176
	v_mad_u32_u16 v18, v234, s92, v176
	v_mad_u32_u16 v22, v235, s92, v176
	global_load_dwordx4 v[2:5], v2, s[28:29]
	global_load_dwordx4 v[6:9], v6, s[28:29]
	global_load_dwordx4 v[18:21], v18, s[28:29]
	global_load_dwordx4 v[22:25], v22, s[28:29]

.Lmk_half_join:
	v_add_f32_e32 v34, v34, v121
	v_mul_f32_e32 v121, 0x3e4ccccd, v34
	v_max_f32_e32 v34, v34, v121
	v_cmp_gt_f32_e32 vcc, v34, v184
	s_and_b64 s[68:69], s[56:57], vcc
	s_cmp_eq_u64 s[68:69], 0
	s_cbranch_scc0 .Lmk_max
	v_add_u32_e32 v229, s82, v172
	v_add_u32_e32 v230, s82, v173
	ds_read2_b32 v[224:225], v229 offset1:8
	ds_read2_b32 v[226:227], v229 offset0:16 offset1:24
	ds_read2_b32 v[232:233], v229 offset0:32 offset1:40
	ds_read2_b32 v[234:235], v229 offset0:48 offset1:56
	v_bfe_u32 v121, v183, 16, 4
	ds_read_b32 v183, v230

.LBB2_110:
.Lmk_gather:
	s_mov_b32 s30, s83
	v_mad_u32_u16 v10, v224, s92, v176
	v_mad_u32_u16 v14, v225, s92, v176
	s_cmp_lt_i32 s83, 17
	global_load_dwordx4 v[10:13], v10, s[28:29]
	global_load_dwordx4 v[14:17], v14, s[28:29]
	s_cbranch_scc1 .LBB2_68
	v_mad_u32_u16 v30, v226, s92, v176
	v_mad_u32_u16 v26, v227, s92, v176
	s_cmp_lt_i32 s83, 33
	global_load_dwordx4 v[30:33], v30, s[28:29]
	global_load_dwordx4 v[26:29], v26, s[28:29]
	s_cbranch_scc1 .LBB2_68
	v_mad_u32_u16 v2, v232, s92, v176
	v_mad_u32_u16 v6, v233, s92, v176
	v_mad_u32_u16 v18, v234, s92, v176
	v_mad_u32_u16 v22, v235, s92, v176
	global_load_dwordx4 v[2:5], v2, s[28:29]
	global_load_dwordx4 v[6:9], v6, s[28:29]
	global_load_dwordx4 v[18:21], v18, s[28:29]
	global_load_dwordx4 v[22:25], v22, s[28:29]

.Lmk_max:
	v_cndmask_b32_e64 v161, v185, v34, s[56:57]
	s_nop 1
	v_max_f32_dpp v161, v161, v161 row_shr:1 row_mask:0xf bank_mask:0xf
	v_bfe_u32 v121, v183, 16, 4
	s_nop 0
	v_max_f32_dpp v161, v161, v161 row_shr:2 row_mask:0xf bank_mask:0xf
	v_add_u32_e32 v229, s82, v172
	v_add_u32_e32 v230, s82, v173
	v_max_f32_dpp v161, v161, v161 row_shr:4 row_mask:0xf bank_mask:0xf
	ds_read2_b32 v[224:225], v229 offset1:8
	s_nop 0
	v_max_f32_dpp v161, v161, v161 row_shr:8 row_mask:0xf bank_mask:0xf
	ds_read2_b32 v[226:227], v229 offset0:16 offset1:24
	s_nop 0
	v_max_f32_dpp v161, v161, v161 row_bcast:15 row_mask:0xa bank_mask:0xf
	ds_read2_b32 v[232:233], v229 offset0:32 offset1:40
	s_nop 0
	v_max_f32_dpp v161, v161, v161 row_bcast:31 row_mask:0xc bank_mask:0xf
	ds_read2_b32 v[234:235], v229 offset0:48 offset1:56
	s_nop 0
	v_readlane_b32 s70, v161, 63
	ds_read_b32 v183, v230
	s_and_b64 vcc, exec, s[54:55]
	s_nop 0
	v_mov_b32_e32 v161, s70
	s_cbranch_vccz .Lmk_rescale

.Lmk_reread:
	v_add_u32_e32 v229, s82, v172
	v_add_u32_e32 v230, s82, v173
	ds_read2_b32 v[224:225], v229 offset1:8
	ds_read2_b32 v[226:227], v229 offset0:16 offset1:24
	ds_read2_b32 v[232:233], v229 offset0:32 offset1:40
	ds_read2_b32 v[234:235], v229 offset0:48 offset1:56
	ds_read_b32 v183, v230
	s_waitcnt lgkmcnt(0)
	s_branch .Lmk_gather
